# P9 unit setup: next unit's slot->token gather goes to LDS by LDS-DMA without a wait (was two waited round trips per unit) + P5 z-wait count fix
# speedup vs baseline: 1.1048x; 1.0009x over previous
.LBB0_939:
	s_mov_b32 s98, 0
	s_nop 0
	v_cndmask_b32_e64 v2, 0, 1, s[4:5]
	v_cmp_ne_u32_e64 s[0:1], 1, v2
	s_andn2_b64 vcc, exec, s[4:5]
	s_mov_b64 s[34:35], s[40:41]
	s_cbranch_vccnz .LBB0_941
	s_ashr_i32 s31, s30, 31
	s_lshl_b64 s[6:7], s[30:31], 23
	s_add_u32 s8, s42, s6
	s_addc_u32 s9, s43, s7
	s_ashr_i32 s29, s28, 31
	s_lshl_b64 s[6:7], s[28:29], 19
	s_add_u32 s34, s8, s6
	s_addc_u32 s35, s9, s7
.LBB0_941:
	s_and_b64 vcc, exec, s[4:5]
	s_cbranch_vccz .LBB0_943
	s_mov_b32 s98, 1
	s_lshl_b32 s4, s30, 2
	s_add_i32 s4, s4, 0
	s_add_i32 s4, s4, 0x23c00
	v_mov_b32_e32 v4, s4
	ds_read_b32 v2, v4 offset:64
	ds_read_b32 v3, v4 offset:256
	s_lshl_b32 s29, s30, 14
	v_readfirstlane_b32 s6, v219
	s_waitcnt lgkmcnt(0)
	v_sub_u32_e32 v2, s64, v2
	v_lshlrev_b32_e32 v2, 8, v2
	v_or_b32_e32 v6, v2, v214
	v_cmp_lt_i32_e32 vcc, v6, v3
	s_mov_b32 m0, s6
	s_add_i32 s6, s6, 0x100
	v_cndmask_b32_e32 v6, 0, v6, vcc
	v_add_u32_e32 v6, s29, v6
	v_ashrrev_i32_e32 v7, 31, v6
	v_lshl_add_u64 v[6:7], v[6:7], 2, s[10:11]
	global_load_lds_dword v[6:7], off
	v_or_b32_e32 v6, v2, v215
	v_cmp_lt_i32_e32 vcc, v6, v3
	s_mov_b32 m0, s6
	s_add_i32 s6, s6, 0x100
	v_cndmask_b32_e32 v6, 0, v6, vcc
	v_add_u32_e32 v6, s29, v6
	v_ashrrev_i32_e32 v7, 31, v6
	v_lshl_add_u64 v[6:7], v[6:7], 2, s[10:11]
	global_load_lds_dword v[6:7], off
	v_or_b32_e32 v6, v2, v216
	v_cmp_lt_i32_e32 vcc, v6, v3
	s_mov_b32 m0, s6
	s_add_i32 s6, s6, 0x100
	v_cndmask_b32_e32 v6, 0, v6, vcc
	v_add_u32_e32 v6, s29, v6
	v_ashrrev_i32_e32 v7, 31, v6
	v_lshl_add_u64 v[6:7], v[6:7], 2, s[10:11]
	global_load_lds_dword v[6:7], off
	v_or_b32_e32 v6, v2, v217
	v_cmp_lt_i32_e32 vcc, v6, v3
	s_mov_b32 m0, s6
	s_add_i32 s6, s6, 0x100
	v_cndmask_b32_e32 v6, 0, v6, vcc
	v_add_u32_e32 v6, s29, v6
	v_ashrrev_i32_e32 v7, 31, v6
	v_lshl_add_u64 v[6:7], v[6:7], 2, s[10:11]
	global_load_lds_dword v[6:7], off

.LBB0_944:
	s_cmp_eq_u32 s98, 0
	s_cbranch_scc1 .Lp9_nonext
	v_bfe_u32 v68, v219, 2, 8
	v_and_b32_e32 v69, 0xfffffc00, v219
	v_add_u32_e32 v68, v68, v69
	ds_read_b32 v71, v68 offset:768
	ds_read_b32 v70, v68 offset:512
	ds_read_b32 v69, v68 offset:256
	ds_read_b32 v68, v68
	v_mov_b32_e32 v211, v67
	s_waitcnt lgkmcnt(0)
	v_lshl_or_b32 v68, v68, 11, v218
	v_lshl_or_b32 v69, v69, 11, v218
	v_lshl_or_b32 v70, v70, 11, v218
	v_lshl_or_b32 v71, v71, 11, v218
	v_mov_b32_e32 v66, v70
	v_mov_b32_e32 v210, v71
	v_mov_b32_e32 v208, v71
	v_mov_b32_e32 v206, v69
	v_mov_b64_e32 v[212:213], v[66:67]
	v_mov_b32_e32 v66, v68

.Lp9_nonext:
	v_mov_b32_e32 v71, v67
	v_mov_b32_e32 v209, v67
	v_mov_b64_e32 v[210:211], v[208:209]
	v_mov_b64_e32 v[212:213], v[70:71]
	s_branch .LBB0_945

	.amdhsa_kernel _Z6mk_fwd4Args
		.amdhsa_group_segment_fixed_size 0
		.amdhsa_private_segment_fixed_size 0
		.amdhsa_kernarg_size 456
		.amdhsa_user_sgpr_count 2
		.amdhsa_user_sgpr_dispatch_ptr 0
		.amdhsa_user_sgpr_queue_ptr 0
		.amdhsa_user_sgpr_kernarg_segment_ptr 1
		.amdhsa_user_sgpr_dispatch_id 0
		.amdhsa_user_sgpr_kernarg_preload_length 0
		.amdhsa_user_sgpr_kernarg_preload_offset 0
		.amdhsa_user_sgpr_private_segment_size 0
		.amdhsa_uses_dynamic_stack 0
		.amdhsa_enable_private_segment 0
		.amdhsa_system_sgpr_workgroup_id_x 1
		.amdhsa_system_sgpr_workgroup_id_y 0
		.amdhsa_system_sgpr_workgroup_id_z 0
		.amdhsa_system_sgpr_workgroup_info 0
		.amdhsa_system_vgpr_workitem_id 0
		.amdhsa_next_free_vgpr 256
		.amdhsa_next_free_sgpr 102
		.amdhsa_accum_offset 256
		.amdhsa_reserve_vcc 1
		.amdhsa_float_round_mode_32 0
		.amdhsa_float_round_mode_16_64 0
		.amdhsa_float_denorm_mode_32 3
		.amdhsa_float_denorm_mode_16_64 3
		.amdhsa_dx10_clamp 1
		.amdhsa_ieee_mode 1
		.amdhsa_fp16_overflow 0
		.amdhsa_tg_split 0
		.amdhsa_exception_fp_ieee_invalid_op 0
		.amdhsa_exception_fp_denorm_src 0
		.amdhsa_exception_fp_ieee_div_zero 0
		.amdhsa_exception_fp_ieee_overflow 0
		.amdhsa_exception_fp_ieee_underflow 0
		.amdhsa_exception_fp_ieee_inexact 0
		.amdhsa_exception_int_div_zero 0
	.end_amdhsa_kernel

amdhsa.kernels:
  - .agpr_count:     0
    .args:
      - .offset:         0
        .size:           200
        .value_kind:     by_value
      - .offset:         200
        .size:           4
        .value_kind:     hidden_block_count_x
      - .offset:         204
        .size:           4
        .value_kind:     hidden_block_count_y
      - .offset:         208
        .size:           4
        .value_kind:     hidden_block_count_z
      - .offset:         212
        .size:           2
        .value_kind:     hidden_group_size_x
      - .offset:         214
        .size:           2
        .value_kind:     hidden_group_size_y
      - .offset:         216
        .size:           2
        .value_kind:     hidden_group_size_z
      - .offset:         218
        .size:           2
        .value_kind:     hidden_remainder_x
      - .offset:         220
        .size:           2
        .value_kind:     hidden_remainder_y
      - .offset:         222
        .size:           2
        .value_kind:     hidden_remainder_z
      - .offset:         240
        .size:           8
        .value_kind:     hidden_global_offset_x
      - .offset:         248
        .size:           8
        .value_kind:     hidden_global_offset_y
      - .offset:         256
        .size:           8
        .value_kind:     hidden_global_offset_z
      - .offset:         264
        .size:           2
        .value_kind:     hidden_grid_dims
      - .offset:         320
        .size:           4
        .value_kind:     hidden_dynamic_lds_size
    .group_segment_fixed_size: 0
    .kernarg_segment_align: 8
    .kernarg_segment_size: 456
    .language:       OpenCL C
    .language_version:
      - 2
      - 0
    .max_flat_workgroup_size: 512
    .name:           _Z6mk_fwd4Args
    .private_segment_fixed_size: 0
    .sgpr_count:     108
    .sgpr_spill_count: 188
    .symbol:         _Z6mk_fwd4Args.kd
    .uniform_work_group_size: 1
    .uses_dynamic_stack: false
    .vgpr_count:     256
    .vgpr_spill_count: 0
    .wavefront_size: 64
